# speedup vs baseline: 1.0480x; 1.0255x over previous
_Z11edge_kernelILi36ELb1EEvPKfS1_PKDF16_PKiS5_S1_S1_S1_S1_S1_PDF16_:
	s_load_dwordx8 s[4:11], s[0:1], 0x0
	s_load_dwordx8 s[12:19], s[0:1], 0x20
	s_load_dwordx4 s[20:23], s[0:1], 0x40
	s_load_dwordx2 s[24:25], s[0:1], 0x50
	v_readfirstlane_b32 s3, v0
	v_bfe_u32 v75, v0, 4, 2
	v_and_b32_e32 v76, 15, v0
	v_and_b32_e32 v78, 63, v0
	s_lshr_b32 s3, s3, 6
	s_lshl_b32 s2, s2, 1
	s_add_i32 s2, s2, s3
	v_lshlrev_b32_e32 v74, 8, v75
	v_lshl_or_b32 v74, v76, 4, v74
	v_lshlrev_b32_e32 v79, 4, v78
	v_lshl_or_b32 v77, v76, 2, v75
	v_lshlrev_b32_e32 v77, 2, v77
	v_mul_u32_u24_e32 v73, 0x900, v75
	v_lshl_or_b32 v73, v76, 4, v73
	v_mul_u32_u24_e32 v78, 36, v75
	s_mul_i32 s28, s2, 0x2400
	s_lshl_b32 s29, s2, 14
	s_lshl_b32 s30, s2, 2
	s_lshl_b32 s31, s2, 8
	s_lshl_b32 s33, s3, 10
	s_lshl_b32 s34, s3, 8
	s_addk_i32 s34, 0x4000
	s_waitcnt lgkmcnt(0)
	s_add_u32 s10, s10, s30
	s_addc_u32 s11, s11, 0
	s_add_u32 s12, s12, s30
	s_addc_u32 s13, s13, 0
	s_load_dword s35, s[10:11], 0x0
	s_load_dword s36, s[12:13], 0x0
	s_add_u32 s14, s14, s28
	s_addc_u32 s15, s15, 0
	global_load_dwordx4 v[0:3], v73, s[14:15] nt
	global_load_dwordx4 v[4:7], v73, s[14:15] offset:256 nt
	global_load_dwordx4 v[8:11], v73, s[14:15] offset:512 nt
	global_load_dwordx4 v[12:15], v73, s[14:15] offset:768 nt
	global_load_dwordx4 v[16:19], v73, s[14:15] offset:1024 nt
	global_load_dwordx4 v[20:23], v73, s[14:15] offset:1280 nt
	global_load_dwordx4 v[24:27], v73, s[14:15] offset:1536 nt
	global_load_dwordx4 v[28:31], v73, s[14:15] offset:1792 nt
	global_load_dwordx4 v[32:35], v73, s[14:15] offset:2048 nt
	s_add_u32 s22, s22, s33
	s_addc_u32 s23, s23, 0
	s_add_u32 s18, s18, s29
	s_addc_u32 s19, s19, 0
	s_add_u32 s16, s16, s31
	s_addc_u32 s17, s17, 0
	s_add_u32 s20, s20, s31
	s_addc_u32 s21, s21, 0
	s_waitcnt lgkmcnt(0)
	s_lshl_b32 s36, s36, 7
	s_add_u32 s24, s24, s36
	s_addc_u32 s25, s25, 0
	s_lshl_b32 s37, s35, 7
	s_lshl_b32 s38, s35, 4
	s_add_u32 s4, s4, s37
	s_addc_u32 s5, s5, 0
	s_add_u32 s6, s6, s38
	s_addc_u32 s7, s7, 0
	v_mov_b32_e32 v93, 0
	v_mov_b32_e32 v92, v78
	v_lshl_add_u64 v[94:95], s[4:5], 0, v[92:93]
	v_lshl_add_u64 v[94:95], v[94:95], 0, 20
	v_cmp_eq_u32_e32 vcc, 3, v75
	s_nop 1
	v_mov_b32_e32 v90, s6
	v_mov_b32_e32 v91, s7
	v_cndmask_b32_e32 v94, v94, v90, vcc
	v_cndmask_b32_e32 v95, v95, v91, vcc
	global_load_dwordx4 v[80:83], v78, s[4:5] nt
	global_load_dword v84, v78, s[4:5] offset:16 nt
	global_load_dwordx4 v[86:89], v[94:95], off nt
	global_load_dword v72, v77, s[16:17] nt
	global_load_dword v64, v77, s[20:21] nt
	s_mov_b32 m0, s33
	s_nop 0
	global_load_lds_dwordx4 v79, s[22:23]
	global_load_lds_dwordx4 v79, s[22:23] offset:2048
	s_add_u32 m0, m0, 0x1000
	s_add_u32 s22, s22, 0x1000
	s_addc_u32 s23, s23, 0
	global_load_lds_dwordx4 v79, s[22:23]
	global_load_lds_dwordx4 v79, s[22:23] offset:2048
	s_add_u32 m0, m0, 0x1000
	s_add_u32 s22, s22, 0x1000
	s_addc_u32 s23, s23, 0
	global_load_lds_dwordx4 v79, s[22:23]
	global_load_lds_dwordx4 v79, s[22:23] offset:2048
	s_add_u32 m0, m0, 0x1000
	s_add_u32 s22, s22, 0x1000
	s_addc_u32 s23, s23, 0
	global_load_lds_dwordx4 v79, s[22:23]
	global_load_lds_dwordx4 v79, s[22:23] offset:2048
	v_add_u32_e32 v78, s34, v77
	v_lshl_add_u32 v79, v75, 2, s34
	s_waitcnt vmcnt(10)
	v_pk_mul_f32 v[96:97], v[80:81], v[0:1] op_sel_hi:[0,1]
	v_pk_mul_f32 v[98:99], v[80:81], v[2:3] op_sel_hi:[0,1]
	v_pk_mul_f32 v[100:101], v[80:81], v[4:5] op_sel:[1,0]
	v_pk_mul_f32 v[102:103], v[80:81], v[6:7] op_sel:[1,0]
	v_pk_fma_f32 v[96:97], v[82:83], v[8:9], v[96:97] op_sel_hi:[0,1,1]
	v_pk_fma_f32 v[98:99], v[82:83], v[10:11], v[98:99] op_sel_hi:[0,1,1]
	v_pk_fma_f32 v[100:101], v[82:83], v[12:13], v[100:101] op_sel:[1,0,0]
	v_pk_fma_f32 v[102:103], v[82:83], v[14:15], v[102:103] op_sel:[1,0,0]
	v_pk_fma_f32 v[96:97], v[84:85], v[16:17], v[96:97] op_sel_hi:[0,1,1]
	v_pk_fma_f32 v[98:99], v[84:85], v[18:19], v[98:99] op_sel_hi:[0,1,1]
	v_pk_fma_f32 v[100:101], v[86:87], v[20:21], v[100:101] op_sel_hi:[0,1,1]
	v_pk_fma_f32 v[102:103], v[86:87], v[22:23], v[102:103] op_sel_hi:[0,1,1]
	v_pk_fma_f32 v[96:97], v[86:87], v[24:25], v[96:97] op_sel:[1,0,0]
	v_pk_fma_f32 v[98:99], v[86:87], v[26:27], v[98:99] op_sel:[1,0,0]
	v_pk_fma_f32 v[100:101], v[88:89], v[28:29], v[100:101] op_sel_hi:[0,1,1]
	v_pk_fma_f32 v[102:103], v[88:89], v[30:31], v[102:103] op_sel_hi:[0,1,1]
	v_pk_fma_f32 v[96:97], v[88:89], v[32:33], v[96:97] op_sel:[1,0,0]
	v_pk_fma_f32 v[98:99], v[88:89], v[34:35], v[98:99] op_sel:[1,0,0]
	v_pk_add_f32 v[96:97], v[96:97], v[100:101]
	v_pk_add_f32 v[98:99], v[98:99], v[102:103]
	s_nop 1
	v_permlane16_swap_b32_e32 v96, v97
	v_permlane16_swap_b32_e32 v98, v99
	v_add_f32_e32 v96, v96, v97
	v_add_f32_e32 v98, v98, v99
	s_nop 1
	v_permlane32_swap_b32_e32 v96, v98
	v_add_f32_e32 v96, v96, v98
	s_waitcnt vmcnt(9)
	v_add_f32_e32 v96, v96, v72
	v_max_f32_e32 v96, 0, v96
	ds_write_b32 v78, v96
	ds_read2_b32 v[80:81], v79 offset0:0 offset1:4
	ds_read2_b32 v[82:83], v79 offset0:8 offset1:12
	ds_read2_b32 v[84:85], v79 offset0:16 offset1:20
	ds_read2_b32 v[86:87], v79 offset0:24 offset1:28
	ds_read2_b32 v[88:89], v79 offset0:32 offset1:36
	ds_read2_b32 v[90:91], v79 offset0:40 offset1:44
	ds_read2_b32 v[92:93], v79 offset0:48 offset1:52
	ds_read2_b32 v[94:95], v79 offset0:56 offset1:60
	s_waitcnt lgkmcnt(0)
	v_cmp_neq_f32_e64 s[40:41], 0, v80
	v_cmp_neq_f32_e64 s[42:43], 0, v81
	v_cmp_neq_f32_e64 s[44:45], 0, v82
	v_cmp_neq_f32_e64 s[46:47], 0, v83
	v_cmp_neq_f32_e64 s[48:49], 0, v84
	v_cmp_neq_f32_e64 s[50:51], 0, v85
	v_cmp_neq_f32_e64 s[52:53], 0, v86
	v_cmp_neq_f32_e64 s[54:55], 0, v87
	v_cmp_neq_f32_e64 s[56:57], 0, v88
	v_cmp_neq_f32_e64 s[58:59], 0, v89
	v_cmp_neq_f32_e64 s[60:61], 0, v90
	v_cmp_neq_f32_e64 s[62:63], 0, v91
	v_cmp_neq_f32_e64 s[64:65], 0, v92
	v_cmp_neq_f32_e64 s[66:67], 0, v93
	v_cmp_neq_f32_e64 s[68:69], 0, v94
	v_cmp_neq_f32_e64 s[70:71], 0, v95
	s_mov_b64 exec, s[40:41]
	global_load_dwordx4 v[0:3], v74, s[18:19] nt
	s_mov_b64 exec, s[42:43]
	global_load_dwordx4 v[4:7], v74, s[18:19] offset:1024 nt
	s_mov_b64 exec, s[44:45]
	global_load_dwordx4 v[8:11], v74, s[18:19] offset:2048 nt
	s_mov_b64 exec, s[46:47]
	global_load_dwordx4 v[12:15], v74, s[18:19] offset:3072 nt
	s_add_u32 s18, s18, 0x1000
	s_addc_u32 s19, s19, 0
	s_mov_b64 exec, s[48:49]
	global_load_dwordx4 v[16:19], v74, s[18:19] nt
	s_mov_b64 exec, s[50:51]
	global_load_dwordx4 v[20:23], v74, s[18:19] offset:1024 nt
	s_mov_b64 exec, s[52:53]
	global_load_dwordx4 v[24:27], v74, s[18:19] offset:2048 nt
	s_mov_b64 exec, s[54:55]
	global_load_dwordx4 v[28:31], v74, s[18:19] offset:3072 nt
	s_add_u32 s18, s18, 0x1000
	s_addc_u32 s19, s19, 0
	s_mov_b64 exec, s[56:57]
	global_load_dwordx4 v[32:35], v74, s[18:19] nt
	s_mov_b64 exec, s[58:59]
	global_load_dwordx4 v[36:39], v74, s[18:19] offset:1024 nt
	s_mov_b64 exec, s[60:61]
	global_load_dwordx4 v[40:43], v74, s[18:19] offset:2048 nt
	s_mov_b64 exec, s[62:63]
	global_load_dwordx4 v[44:47], v74, s[18:19] offset:3072 nt
	s_add_u32 s18, s18, 0x1000
	s_addc_u32 s19, s19, 0
	s_mov_b64 exec, s[64:65]
	global_load_dwordx4 v[48:51], v74, s[18:19] nt
	s_mov_b64 exec, s[66:67]
	global_load_dwordx4 v[52:55], v74, s[18:19] offset:1024 nt
	s_mov_b64 exec, s[68:69]
	global_load_dwordx4 v[56:59], v74, s[18:19] offset:2048 nt
	s_mov_b64 exec, s[70:71]
	global_load_dwordx4 v[60:63], v74, s[18:19] offset:3072 nt
	s_mov_b64 exec, -1
	v_mov_b32_e32 v96, 0
	v_mov_b32_e32 v97, 0
	v_mov_b32_e32 v98, 0
	v_mov_b32_e32 v99, 0
	v_mov_b32_e32 v100, 0
	v_mov_b32_e32 v101, 0
	v_mov_b32_e32 v102, 0
	v_mov_b32_e32 v103, 0
	s_waitcnt vmcnt(0)
	s_barrier
	s_mov_b64 exec, s[40:41]
	v_pk_fma_f32 v[96:97], v[80:81], v[0:1], v[96:97] op_sel_hi:[0,1,1]
	v_pk_fma_f32 v[98:99], v[80:81], v[2:3], v[98:99] op_sel_hi:[0,1,1]
	s_mov_b64 exec, s[42:43]
	v_pk_fma_f32 v[100:101], v[80:81], v[4:5], v[100:101] op_sel:[1,0,0]
	v_pk_fma_f32 v[102:103], v[80:81], v[6:7], v[102:103] op_sel:[1,0,0]
	s_mov_b64 exec, s[44:45]
	v_pk_fma_f32 v[96:97], v[82:83], v[8:9], v[96:97] op_sel_hi:[0,1,1]
	v_pk_fma_f32 v[98:99], v[82:83], v[10:11], v[98:99] op_sel_hi:[0,1,1]
	s_mov_b64 exec, s[46:47]
	v_pk_fma_f32 v[100:101], v[82:83], v[12:13], v[100:101] op_sel:[1,0,0]
	v_pk_fma_f32 v[102:103], v[82:83], v[14:15], v[102:103] op_sel:[1,0,0]
	s_mov_b64 exec, s[48:49]
	v_pk_fma_f32 v[96:97], v[84:85], v[16:17], v[96:97] op_sel_hi:[0,1,1]
	v_pk_fma_f32 v[98:99], v[84:85], v[18:19], v[98:99] op_sel_hi:[0,1,1]
	s_mov_b64 exec, s[50:51]
	v_pk_fma_f32 v[100:101], v[84:85], v[20:21], v[100:101] op_sel:[1,0,0]
	v_pk_fma_f32 v[102:103], v[84:85], v[22:23], v[102:103] op_sel:[1,0,0]
	s_mov_b64 exec, s[52:53]
	v_pk_fma_f32 v[96:97], v[86:87], v[24:25], v[96:97] op_sel_hi:[0,1,1]
	v_pk_fma_f32 v[98:99], v[86:87], v[26:27], v[98:99] op_sel_hi:[0,1,1]
	s_mov_b64 exec, s[54:55]
	v_pk_fma_f32 v[100:101], v[86:87], v[28:29], v[100:101] op_sel:[1,0,0]
	v_pk_fma_f32 v[102:103], v[86:87], v[30:31], v[102:103] op_sel:[1,0,0]
	s_mov_b64 exec, s[56:57]
	v_pk_fma_f32 v[96:97], v[88:89], v[32:33], v[96:97] op_sel_hi:[0,1,1]
	v_pk_fma_f32 v[98:99], v[88:89], v[34:35], v[98:99] op_sel_hi:[0,1,1]
	s_mov_b64 exec, s[58:59]
	v_pk_fma_f32 v[100:101], v[88:89], v[36:37], v[100:101] op_sel:[1,0,0]
	v_pk_fma_f32 v[102:103], v[88:89], v[38:39], v[102:103] op_sel:[1,0,0]
	s_mov_b64 exec, s[60:61]
	v_pk_fma_f32 v[96:97], v[90:91], v[40:41], v[96:97] op_sel_hi:[0,1,1]
	v_pk_fma_f32 v[98:99], v[90:91], v[42:43], v[98:99] op_sel_hi:[0,1,1]
	s_mov_b64 exec, s[62:63]
	v_pk_fma_f32 v[100:101], v[90:91], v[44:45], v[100:101] op_sel:[1,0,0]
	v_pk_fma_f32 v[102:103], v[90:91], v[46:47], v[102:103] op_sel:[1,0,0]
	s_mov_b64 exec, s[64:65]
	v_pk_fma_f32 v[96:97], v[92:93], v[48:49], v[96:97] op_sel_hi:[0,1,1]
	v_pk_fma_f32 v[98:99], v[92:93], v[50:51], v[98:99] op_sel_hi:[0,1,1]
	s_mov_b64 exec, s[66:67]
	v_pk_fma_f32 v[100:101], v[92:93], v[52:53], v[100:101] op_sel:[1,0,0]
	v_pk_fma_f32 v[102:103], v[92:93], v[54:55], v[102:103] op_sel:[1,0,0]
	s_mov_b64 exec, s[68:69]
	v_pk_fma_f32 v[96:97], v[94:95], v[56:57], v[96:97] op_sel_hi:[0,1,1]
	v_pk_fma_f32 v[98:99], v[94:95], v[58:59], v[98:99] op_sel_hi:[0,1,1]
	s_mov_b64 exec, s[70:71]
	v_pk_fma_f32 v[100:101], v[94:95], v[60:61], v[100:101] op_sel:[1,0,0]
	v_pk_fma_f32 v[102:103], v[94:95], v[62:63], v[102:103] op_sel:[1,0,0]
	s_mov_b64 exec, -1
	ds_read_b128 v[0:3], v74
	ds_read_b128 v[4:7], v74 offset:1024
	ds_read_b128 v[8:11], v74 offset:2048
	ds_read_b128 v[12:15], v74 offset:3072
	ds_read_b128 v[16:19], v74 offset:4096
	ds_read_b128 v[20:23], v74 offset:5120
	ds_read_b128 v[24:27], v74 offset:6144
	ds_read_b128 v[28:31], v74 offset:7168
	ds_read_b128 v[32:35], v74 offset:8192
	ds_read_b128 v[36:39], v74 offset:9216
	ds_read_b128 v[40:43], v74 offset:10240
	ds_read_b128 v[44:47], v74 offset:11264
	ds_read_b128 v[48:51], v74 offset:12288
	ds_read_b128 v[52:55], v74 offset:13312
	ds_read_b128 v[56:59], v74 offset:14336
	v_pk_add_f32 v[96:97], v[96:97], v[100:101]
	v_pk_add_f32 v[98:99], v[98:99], v[102:103]
	s_nop 1
	v_permlane16_swap_b32_e32 v96, v97
	v_permlane16_swap_b32_e32 v98, v99
	v_add_f32_e32 v96, v96, v97
	v_add_f32_e32 v98, v98, v99
	s_nop 1
	v_permlane32_swap_b32_e32 v96, v98
	v_add_f32_e32 v96, v96, v98
	v_add_f32_e32 v96, v96, v64
	s_waitcnt lgkmcnt(5)
	ds_read_b128 v[60:63], v74 offset:15360
	ds_write_b32 v78, v96
	ds_read2_b32 v[80:81], v79 offset0:0 offset1:4
	ds_read2_b32 v[82:83], v79 offset0:8 offset1:12
	ds_read2_b32 v[84:85], v79 offset0:16 offset1:20
	ds_read2_b32 v[86:87], v79 offset0:24 offset1:28
	ds_read2_b32 v[88:89], v79 offset0:32 offset1:36
	ds_read2_b32 v[90:91], v79 offset0:40 offset1:44
	ds_read2_b32 v[92:93], v79 offset0:48 offset1:52
	ds_read2_b32 v[94:95], v79 offset0:56 offset1:60
	v_lshlrev_b32_e32 v72, 3, v76
	v_lshl_or_b32 v72, v75, 2, v72
	v_cmp_gt_u32_e32 vcc, 2, v75
	s_waitcnt lgkmcnt(0)
	v_pk_mul_f32 v[96:97], v[80:81], v[0:1] op_sel_hi:[0,1]
	v_pk_mul_f32 v[98:99], v[80:81], v[2:3] op_sel_hi:[0,1]
	v_pk_mul_f32 v[100:101], v[80:81], v[4:5] op_sel:[1,0]
	v_pk_mul_f32 v[102:103], v[80:81], v[6:7] op_sel:[1,0]
	v_pk_fma_f32 v[96:97], v[82:83], v[8:9], v[96:97] op_sel_hi:[0,1,1]
	v_pk_fma_f32 v[98:99], v[82:83], v[10:11], v[98:99] op_sel_hi:[0,1,1]
	v_pk_fma_f32 v[100:101], v[82:83], v[12:13], v[100:101] op_sel:[1,0,0]
	v_pk_fma_f32 v[102:103], v[82:83], v[14:15], v[102:103] op_sel:[1,0,0]
	v_pk_fma_f32 v[96:97], v[84:85], v[16:17], v[96:97] op_sel_hi:[0,1,1]
	v_pk_fma_f32 v[98:99], v[84:85], v[18:19], v[98:99] op_sel_hi:[0,1,1]
	v_pk_fma_f32 v[100:101], v[84:85], v[20:21], v[100:101] op_sel:[1,0,0]
	v_pk_fma_f32 v[102:103], v[84:85], v[22:23], v[102:103] op_sel:[1,0,0]
	v_pk_fma_f32 v[96:97], v[86:87], v[24:25], v[96:97] op_sel_hi:[0,1,1]
	v_pk_fma_f32 v[98:99], v[86:87], v[26:27], v[98:99] op_sel_hi:[0,1,1]
	v_pk_fma_f32 v[100:101], v[86:87], v[28:29], v[100:101] op_sel:[1,0,0]
	v_pk_fma_f32 v[102:103], v[86:87], v[30:31], v[102:103] op_sel:[1,0,0]
	v_pk_fma_f32 v[96:97], v[88:89], v[32:33], v[96:97] op_sel_hi:[0,1,1]
	v_pk_fma_f32 v[98:99], v[88:89], v[34:35], v[98:99] op_sel_hi:[0,1,1]
	v_pk_fma_f32 v[100:101], v[88:89], v[36:37], v[100:101] op_sel:[1,0,0]
	v_pk_fma_f32 v[102:103], v[88:89], v[38:39], v[102:103] op_sel:[1,0,0]
	v_pk_fma_f32 v[96:97], v[90:91], v[40:41], v[96:97] op_sel_hi:[0,1,1]
	v_pk_fma_f32 v[98:99], v[90:91], v[42:43], v[98:99] op_sel_hi:[0,1,1]
	v_pk_fma_f32 v[100:101], v[90:91], v[44:45], v[100:101] op_sel:[1,0,0]
	v_pk_fma_f32 v[102:103], v[90:91], v[46:47], v[102:103] op_sel:[1,0,0]
	v_pk_fma_f32 v[96:97], v[92:93], v[48:49], v[96:97] op_sel_hi:[0,1,1]
	v_pk_fma_f32 v[98:99], v[92:93], v[50:51], v[98:99] op_sel_hi:[0,1,1]
	v_pk_fma_f32 v[100:101], v[92:93], v[52:53], v[100:101] op_sel:[1,0,0]
	v_pk_fma_f32 v[102:103], v[92:93], v[54:55], v[102:103] op_sel:[1,0,0]
	v_pk_fma_f32 v[96:97], v[94:95], v[56:57], v[96:97] op_sel_hi:[0,1,1]
	v_pk_fma_f32 v[98:99], v[94:95], v[58:59], v[98:99] op_sel_hi:[0,1,1]
	v_pk_fma_f32 v[100:101], v[94:95], v[60:61], v[100:101] op_sel:[1,0,0]
	v_pk_fma_f32 v[102:103], v[94:95], v[62:63], v[102:103] op_sel:[1,0,0]
	v_pk_add_f32 v[96:97], v[96:97], v[100:101]
	v_pk_add_f32 v[98:99], v[98:99], v[102:103]
	s_nop 1
	v_permlane16_swap_b32_e32 v96, v98
	v_permlane16_swap_b32_e32 v97, v99
	v_add_f32_e32 v96, v96, v98
	v_add_f32_e32 v97, v97, v99
	v_mov_b32_e32 v80, v96
	v_mov_b32_e32 v81, v97
	s_nop 1
	v_permlane32_swap_b32_e32 v96, v80
	v_permlane32_swap_b32_e32 v97, v81
	v_add_f32_e32 v96, v96, v80
	v_add_f32_e32 v97, v97, v81
	v_cvt_pk_f16_f32 v73, v96, v97
	s_and_saveexec_b64 s[4:5], vcc
	global_atomic_pk_add_f16 v72, v73, s[24:25]
	s_endpgm
	.p2align	8
